# speedup vs baseline: 1.0036x; 1.0024x over previous
.Lp_next:
	s_setprio 2
	s_mov_b64 exec, 1
	ds_add_rtn_u32 v10, v59, v60
	s_mov_b64 exec, -1
	s_waitcnt lgkmcnt(0)
	v_readfirstlane_b32 s34, v10
	s_cmp_lt_u32 s34, s62
	s_cselect_b32 s45, s64, s65
	s_cselect_b32 s46, 0, s62
	s_cselect_b32 s48, s62, s63
	s_sub_u32 s47, s34, s46
	s_cmp_ge_u32 s47, s48
	s_cbranch_scc1 .Lp_done
	s_lshl_b32 s47, s47, 3
	s_add_u32 s45, s45, s47
	v_mov_b32_e32 v11, s45
	ds_read2_b32 v[12:13], v11 offset1:1
	s_waitcnt lgkmcnt(0)
	v_readfirstlane_b32 s35, v12
	v_readfirstlane_b32 s36, v13
	s_nop 1
	v_mov_b32_e32 v10, s35
	v_mov_b32_e32 v11, s36
	v_cndmask_b32_e64 v12, v10, v11, s[54:55]
	v_cndmask_b32_e64 v13, v10, v11, s[56:57]
	v_lshl_add_u32 v12, v12, 3, v61
	v_lshl_add_u32 v14, v13, 4, v62
	ds_read_b64 v[2:3], v12
	ds_read_b128 v[4:7], v14
	v_mad_u32_u24 v9, v13, s49, v58
	v_mov_b32_e32 v8, v56
	s_waitcnt lgkmcnt(0)
	v_add_u32_e32 v2, v2, v55
	v_and_b32_e32 v3, v3, v63
	s_nop 0
	v_readlane_b32 s41, v3, 0
	v_readlane_b32 s42, v3, 4
	s_max_u32 s43, s41, s42
	s_cmp_eq_u32 s43, 0
	s_cbranch_scc1 .Lp_zero
	ds_read_b64 v[36:37], v2
	v_cmp_gt_u32_e32 vcc, v3, v8
	v_add_u32_e32 v2, 64, v2
	v_add_u32_e32 v8, 16, v8
	v_mov_b32_e32 v33, 0x3c00
	s_waitcnt lgkmcnt(0)
	v_perm_b32 v32, v37, v36, v57
	v_cndmask_b32_e32 v33, 0, v33, vcc
	s_nop 0
	v_cndmask_b32_e32 v32, 0, v32, vcc
	s_nop 1
	v_mfma_f32_32x32x16_f16 v[96:111], v[32:35], v[64:67], 0
	v_mfma_f32_32x32x16_f16 v[112:127], v[32:35], v[68:71], 0
	s_setprio 0
	s_nop 10
	s_mov_b32 s45, s43
	s_min_u32 s46, s45, 16
	s_add_i32 s46, s46, 3
	s_lshr_b32 s46, s46, 2
	s_cmp_eq_u32 s46, 4
	s_cbranch_scc1 .Lf4
	s_cmp_eq_u32 s46, 3
	s_cbranch_scc1 .Lf3
	s_cmp_eq_u32 s46, 2
	s_cbranch_scc1 .Lf2

.Lsub:
	s_setprio 2
	ds_read_b64 v[36:37], v2
	v_cmp_gt_u32_e32 vcc, v3, v8
	v_add_u32_e32 v2, 64, v2
	v_add_u32_e32 v8, 16, v8
	v_mov_b32_e32 v33, 0x3c00
	s_waitcnt lgkmcnt(0)
	v_perm_b32 v32, v37, v36, v57
	v_cndmask_b32_e32 v33, 0, v33, vcc
	s_nop 0
	v_cndmask_b32_e32 v32, 0, v32, vcc
	s_nop 1
	v_mfma_f32_32x32x16_f16 v[96:111], v[32:35], v[64:67], 0
	v_mfma_f32_32x32x16_f16 v[112:127], v[32:35], v[68:71], 0
	s_setprio 0
	s_nop 10
	s_sub_u32 s45, s43, s44
	s_min_u32 s46, s45, 16
	s_add_i32 s46, s46, 3
	s_lshr_b32 s46, s46, 2
	s_cmp_eq_u32 s46, 4
	s_cbranch_scc1 .Ln4
	s_cmp_eq_u32 s46, 3
	s_cbranch_scc1 .Ln3
	s_cmp_eq_u32 s46, 2
	s_cbranch_scc1 .Ln2

.Lp_done:
	s_setprio 0
	v_xor_b32_e32 v102, 16, v18
	v_lshlrev_b32_e32 v102, 2, v102
	s_branch .LBB3_67
